# E phase: 64-lane sums via DPP reduction + readlane broadcast instead of 6-hop ds_bpermute butterflies
# speedup vs baseline: 1.0044x; 1.0044x over previous
; __device__ __forceinline__ float lo16(unsigned u) { return __uint_as_float(u << 16); }
; __device__ __forceinline__ float hi16(unsigned u) { return __uint_as_float(u & 0xffff0000u); }
; __device__ __forceinline__ float wave_sum(float v) {
; #pragma unroll
;     for (int o = 32; o >= 1; o >>= 1) v += __shfl_xor(v, o);
;     return v;
; }
; __device__ void phase_E_rows(const Params& p, int l, char* smem, int vb, int nvb, bool split, int nrows, int oz) {
;     ...
;         float y[4][4];
;         float ss = 0.f;
; #pragma unroll
;         for (int k = 0; k < 4; ++k) {
;             { const u32x4 w = yq[k >> 1]; const int h2 = 2 * (k & 1); y[k][0] = lo16(w[h2]); y[k][1] = hi16(w[h2]); y[k][2] = lo16(w[h2 + 1]); y[k][3] = hi16(w[h2 + 1]); }
;             ss += y[k][0] * y[k][0] + y[k][1] * y[k][1] + y[k][2] * y[k][2] + y[k][3] * y[k][3];
;         }
;         float rs = 0.f;
;         if (l > 0) {
;             ss = wave_sum(ss);
;             rs = rsqrtf(ss * (1.f / DM) + EPS);
;         }
.LBB0_957:
	v_lshlrev_b32_e32 v174, 16, v48
	v_and_b32_e32 v175, 0xffff0000, v48
	v_lshlrev_b32_e32 v172, 16, v49
	v_and_b32_e32 v173, 0xffff0000, v49
	v_lshlrev_b32_e32 v170, 16, v50
	v_and_b32_e32 v171, 0xffff0000, v50
	v_lshlrev_b32_e32 v168, 16, v51
	v_and_b32_e32 v169, 0xffff0000, v51
	v_lshlrev_b32_e32 v166, 16, v44
	v_and_b32_e32 v167, 0xffff0000, v44
	v_lshlrev_b32_e32 v50, 16, v45
	v_and_b32_e32 v51, 0xffff0000, v45
	v_lshlrev_b32_e32 v48, 16, v46
	v_and_b32_e32 v49, 0xffff0000, v46
	v_lshlrev_b32_e32 v44, 16, v47
	s_and_b64 vcc, exec, s[44:45]
	v_and_b32_e32 v45, 0xffff0000, v47
	s_cbranch_vccnz .LBB0_959
	v_mov_b32_e32 v180, v175
	v_mov_b32_e32 v181, v171
	v_mov_b32_e32 v178, v174
	v_mov_b32_e32 v179, v170
	v_pk_mul_f32 v[180:181], v[180:181], v[180:181]
	v_mov_b32_e32 v176, v172
	v_mov_b32_e32 v177, v168
	v_pk_fma_f32 v[178:179], v[178:179], v[178:179], v[180:181]
	v_mov_b32_e32 v46, v173
	v_mov_b32_e32 v47, v169
	v_pk_fma_f32 v[176:177], v[176:177], v[176:177], v[178:179]
	v_mov_b32_e32 v182, v49
	v_mov_b32_e32 v183, v167
	v_pk_fma_f32 v[46:47], v[46:47], v[46:47], v[176:177]
	v_mov_b32_e32 v180, v48
	v_mov_b32_e32 v181, v166
	v_pk_mul_f32 v[182:183], v[182:183], v[182:183]
	v_mov_b32_e32 v178, v44
	v_mov_b32_e32 v179, v50
	v_pk_fma_f32 v[180:181], v[180:181], v[180:181], v[182:183]
	v_add_f32_e32 v46, v46, v47
	v_mov_b32_e32 v176, v45
	v_mov_b32_e32 v177, v51
	v_pk_fma_f32 v[178:179], v[178:179], v[178:179], v[180:181]
	v_pk_fma_f32 v[176:177], v[176:177], v[176:177], v[178:179]
	v_add_f32_e32 v46, v177, v46
	v_add_f32_e32 v46, v176, v46
	s_nop 1
	v_add_f32_dpp v47, v46, v46 quad_perm:[1,0,3,2] row_mask:0xf bank_mask:0xf
	s_nop 1
	v_add_f32_dpp v46, v47, v47 quad_perm:[2,3,0,1] row_mask:0xf bank_mask:0xf
	s_nop 1
	v_add_f32_dpp v47, v46, v46 row_half_mirror row_mask:0xf bank_mask:0xf
	s_nop 1
	v_add_f32_dpp v46, v47, v47 row_mirror row_mask:0xf bank_mask:0xf
	s_nop 1
	v_add_f32_dpp v46, v46, v46 row_bcast:15 row_mask:0xa bank_mask:0xf
	s_nop 1
	v_add_f32_dpp v46, v46, v46 row_bcast:31 row_mask:0xc bank_mask:0xf
	s_nop 1
	v_readlane_b32 s96, v46, 63
	s_nop 1
	v_mov_b32_e32 v46, s96
	v_fmamk_f32 v46, v46, 0x3a800000, v196
	v_mul_f32_e32 v47, 0x4b800000, v46
	v_cmp_gt_f32_e32 vcc, s63, v46
	s_nop 1
	v_cndmask_b32_e32 v46, v46, v47, vcc
	v_rsq_f32_e32 v46, v46
	s_nop 0
	v_mul_f32_e32 v47, 0x45800000, v46
	v_cndmask_b32_e32 v46, v46, v47, vcc
	s_branch .LBB0_960

; __device__ void phase_E_rows(const Params& p, int l, char* smem, int vb, int nvb, bool split, int nrows, int oz) {
;     ...
;         if (l < 4) {
;             ss2 = wave_sum(ss2);
;             const float rs2 = rsqrtf(ss2 * (1.f / DM) + EPS);
;             const __amdgpu_buffer_rsrc_t hr = __builtin_amdgcn_make_buffer_rsrc((void*)(P + (size_t)row * DM), (short)0, 2048, 0x00020000);
; #pragma unroll
;             for (int k2 = 0; k2 < 2; ++k2) {
;                 u32x4 hv;
; #pragma unroll
;                 for (int hh = 0; hh < 2; ++hh) {
;                     const int k = 2 * k2 + hh;
;                     hv[2 * hh] = cvt_pk(xv[k].x * rs2 * pa[k].x + sh[k].x, xv[k].y * rs2 * pa[k].y + sh[k].y);
;                     hv[2 * hh + 1] = cvt_pk(xv[k].z * rs2 * pa[k].z + sh[k].z, xv[k].w * rs2 * pa[k].w + sh[k].w);
;                 }
;                 __builtin_amdgcn_raw_buffer_store_b128(hv, hr, (k2 * 512 + lane * 8) * 2, 0, 16);
;             }
;         }
.LBB0_962:
	s_andn2_b64 vcc, exec, s[50:51]
	s_cbranch_vccnz .LBB0_964
	v_pk_mul_f32 v[36:37], v[26:27], v[26:27]
	v_pk_mul_f32 v[40:41], v[30:31], v[30:31]
	v_pk_mul_f32 v[38:39], v[20:21], v[20:21]
	v_pk_mul_f32 v[42:43], v[22:23], v[22:23]
	v_pk_mul_f32 v[44:45], v[32:33], v[32:33]
	v_add_f32_e32 v40, v41, v40
	v_add_f32_e32 v36, v37, v36
	v_pk_mul_f32 v[46:47], v[24:25], v[24:25]
	v_add_f32_e32 v40, v42, v40
	v_add_f32_e32 v36, v38, v36
	v_add_f32_e32 v37, v45, v44
	v_add_f32_e32 v40, v43, v40
	v_add_f32_e32 v36, v39, v36
	v_add_f32_e32 v37, v46, v37
	v_pk_mul_f32 v[48:49], v[34:35], v[34:35]
	v_add_f32_e32 v36, v36, v40
	v_add_f32_e32 v37, v47, v37
	v_pk_mul_f32 v[50:51], v[28:29], v[28:29]
	v_add_f32_e32 v36, v36, v37
	v_add_f32_e32 v37, v49, v48
	v_add_f32_e32 v37, v50, v37
	v_add_f32_e32 v37, v51, v37
	v_add_f32_e32 v36, v36, v37
	s_and_b32 s29, s65, 0xffff
	s_mov_b32 s28, s64
	s_mov_b32 s31, s23
	s_nop 1
	v_add_f32_dpp v37, v36, v36 quad_perm:[1,0,3,2] row_mask:0xf bank_mask:0xf
	s_nop 1
	v_add_f32_dpp v36, v37, v37 quad_perm:[2,3,0,1] row_mask:0xf bank_mask:0xf
	s_nop 1
	v_add_f32_dpp v37, v36, v36 row_half_mirror row_mask:0xf bank_mask:0xf
	s_nop 1
	v_add_f32_dpp v36, v37, v37 row_mirror row_mask:0xf bank_mask:0xf
	s_nop 1
	v_add_f32_dpp v36, v36, v36 row_bcast:15 row_mask:0xa bank_mask:0xf
	s_nop 1
	v_add_f32_dpp v36, v36, v36 row_bcast:31 row_mask:0xc bank_mask:0xf
	s_nop 1
	v_readlane_b32 s96, v36, 63
	s_nop 1
	v_mov_b32_e32 v36, s96
	v_fmamk_f32 v36, v36, 0x3a800000, v196
	v_mul_f32_e32 v37, 0x4b800000, v36
	v_cmp_gt_f32_e32 vcc, s63, v36
	s_nop 1
	v_cndmask_b32_e32 v36, v36, v37, vcc
	v_rsq_f32_e32 v36, v36
	s_nop 0
	v_mul_f32_e32 v37, 0x45800000, v36
	v_cndmask_b32_e32 v40, v36, v37, vcc
	v_pk_mul_f32 v[20:21], v[20:21], v[40:41] op_sel_hi:[1,0]
	v_pk_mul_f32 v[26:27], v[26:27], v[40:41] op_sel_hi:[1,0]
	v_pk_fma_f32 v[20:21], v[130:131], v[20:21], v[6:7]
	v_pk_fma_f32 v[26:27], v[132:133], v[26:27], v[4:5]
	v_cvt_pk_bf16_f32 v37, v20, v21
	v_pk_mul_f32 v[20:21], v[30:31], v[40:41] op_sel_hi:[1,0]
	v_cvt_pk_bf16_f32 v36, v26, v27
	v_pk_fma_f32 v[20:21], v[140:141], v[20:21], v[8:9]
	s_nop 0
	v_cvt_pk_bf16_f32 v38, v20, v21
	v_pk_mul_f32 v[20:21], v[22:23], v[40:41] op_sel_hi:[1,0]
	v_pk_mul_f32 v[22:23], v[24:25], v[40:41] op_sel_hi:[1,0]
	v_pk_fma_f32 v[20:21], v[138:139], v[20:21], v[10:11]
	v_pk_fma_f32 v[22:23], v[142:143], v[22:23], v[14:15]
	v_cvt_pk_bf16_f32 v39, v20, v21
	v_pk_mul_f32 v[20:21], v[32:33], v[40:41] op_sel_hi:[1,0]
	v_pk_mul_f32 v[24:25], v[28:29], v[40:41] op_sel_hi:[1,0]
	v_pk_fma_f32 v[20:21], v[144:145], v[20:21], v[12:13]
	v_pk_fma_f32 v[24:25], v[148:149], v[24:25], v[18:19]
	v_cvt_pk_bf16_f32 v20, v20, v21
	v_cvt_pk_bf16_f32 v21, v22, v23
	v_pk_mul_f32 v[22:23], v[34:35], v[40:41] op_sel_hi:[1,0]
	buffer_store_dwordx4 v[36:39], v102, s[28:31], 0 offen sc1
	v_pk_fma_f32 v[22:23], v[146:147], v[22:23], v[16:17]
	s_nop 0
	v_cvt_pk_bf16_f32 v22, v22, v23
	v_cvt_pk_bf16_f32 v23, v24, v25
	buffer_store_dwordx4 v[20:23], v103, s[28:31], 0 offen sc1
